# v85 + nt on the 24 scan-record stores of P4 (235 MB streamed once to the scan much later)
# baseline (speedup 1.0000x reference)
; __device__ __forceinline__ unsigned pk2(float lo, float hi) { return f2bf(lo) | (f2bf(hi) << 16); }
; __device__ __forceinline__ f32x4 bf4(v2u w) { return (f32x4){bflo(w.x), bfhi(w.x), bflo(w.y), bfhi(w.y)}; }
; __device__ __forceinline__ void p4_rwkv_prep(Frame& F) {
;     ...
;         for (int k = 0; k < 4; ++k) { const int t = tb + k * tstep;
;             if (t < S_) {
;                 const f32x4 rc = bf4(zcr[k]), kc = bf4(zck[k]), vc = bf4(zcv[k]);
;                 f32x4 rp = {0.f, 0.f, 0.f, 0.f}, kp = rp, vp = rp;
;                 if (t > 0) { rp = bf4(zpr[k]); kp = bf4(zpk[k]); vp = bf4(zpv[k]); }
;                 const f32x4 r = rc + (rp - rc) * mur, kx = kc + (kp - kc) * muk, v = vc + (vp - vc) * muv;
;                 const f32x4 iclr = bf4(ic[k]), w = wd[k];
;                 f32x4 kk = kx * kk4;
;                 const float ss = dpp_add16((kk.x * kk.x + kk.y * kk.y) + (kk.z * kk.z + kk.w * kk.w)); kk = kk * (1.0f / sqrtf(ss + 1e-12f));
;                 const f32x4 km = kx * (1.0f + (iclr - 1.0f) * ka4);
;                 const f32x4 rkr = r * km * rk4;
;                 const float bc = dpp_add16((rkr.x + rkr.y) + (rkr.z + rkr.w));
;                 unsigned char* rec = SC + ((size_t)h * S_ + t) * SCAN_REC;
;                 *(f32x4*)(rec + 16 * q) = w;
;                 const f32x4 a = -kk, b = kk * iclr;
;                 *(v2u*)(rec + 256 + 8 * q) = (v2u){pk2(r.x, r.y), pk2(r.z, r.w)};
;                 *(v2u*)(rec + 384 + 8 * q) = (v2u){pk2(km.x, km.y), pk2(km.z, km.w)};
;                 *(v2u*)(rec + 512 + 8 * q) = (v2u){pk2(v.x, v.y), pk2(v.z, v.w)};
;                 *(v2u*)(rec + 640 + 8 * q) = (v2u){pk2(a.x, a.y), pk2(a.z, a.w)};
;                 *(v2u*)(rec + 768 + 8 * q) = (v2u){pk2(b.x, b.y), pk2(b.z, b.w)};
;                 if (q == 0) BC[t * RH + h] = bc; } }
.LBB0_1871:
	s_waitcnt vmcnt(2)
	v_lshlrev_b32_e32 v120, 16, v116
	v_and_b32_e32 v121, 0xffff0000, v116
	v_lshlrev_b32_e32 v116, 16, v117
	v_and_b32_e32 v117, 0xffff0000, v117
	v_lshlrev_b32_e32 v134, 16, v114
	v_and_b32_e32 v135, 0xffff0000, v114
	v_lshlrev_b32_e32 v114, 16, v115
	v_and_b32_e32 v115, 0xffff0000, v115
	v_sub_f32_e32 v139, v131, v121
	v_sub_f32_e32 v131, v132, v117
	v_sub_f32_e32 v130, v130, v116
	v_sub_f32_e32 v138, v129, v120
	v_pk_fma_f32 v[116:117], v[4:5], v[130:131], v[116:117]
	v_sub_f32_e32 v131, v127, v135
	v_sub_f32_e32 v130, v122, v134
	v_sub_f32_e32 v129, v128, v115
	v_sub_f32_e32 v128, v123, v114
	v_pk_fma_f32 v[114:115], v[8:9], v[128:129], v[114:115]
	v_pk_fma_f32 v[122:123], v[6:7], v[130:131], v[134:135]
	v_pk_mul_f32 v[132:133], v[16:17], v[114:115]
	v_pk_mul_f32 v[130:131], v[14:15], v[122:123]
	v_pk_fma_f32 v[120:121], v[2:3], v[138:139], v[120:121]
	v_pk_mul_f32 v[134:135], v[132:133], v[132:133]
	v_pk_mul_f32 v[138:139], v[130:131], v[130:131]
	v_lshlrev_b32_e32 v136, 16, v112
	v_pk_mov_b32 v[140:141], v[138:139], v[134:135] op_sel:[1,0]
	v_mov_b32_e32 v139, v135
	v_pk_add_f32 v[134:135], v[140:141], v[138:139]
	v_sub_f32_e32 v128, v55, v136
	v_add_f32_e32 v55, v134, v135
	v_and_b32_e32 v137, 0xffff0000, v112
	v_lshlrev_b32_e32 v112, 16, v113
	v_add_f32_dpp v55, v55, v55 quad_perm:[1,0,3,2] row_mask:0xf bank_mask:0xf bound_ctrl:1
	v_sub_f32_e32 v129, v118, v137
	v_sub_f32_e32 v118, v57, v112
	v_add_f32_dpp v55, v55, v55 quad_perm:[2,3,0,1] row_mask:0xf bank_mask:0xf bound_ctrl:1
	v_and_b32_e32 v113, 0xffff0000, v113
	v_sub_f32_e32 v119, v119, v113
	v_add_f32_dpp v55, v55, v55 row_half_mirror row_mask:0xf bank_mask:0xf bound_ctrl:1
	v_pk_fma_f32 v[112:113], v[12:13], v[118:119], v[112:113]
	v_pk_fma_f32 v[118:119], v[10:11], v[128:129], v[136:137]
	v_add_f32_dpp v55, v55, v55 row_mirror row_mask:0xf bank_mask:0xf bound_ctrl:1
	v_add_f32_e32 v55, 0x2b8cbccc, v55
	v_mul_f32_e32 v57, 0x4f800000, v55
	v_cmp_gt_f32_e32 vcc, s29, v55
	s_waitcnt vmcnt(1)
	v_lshlrev_b32_e32 v128, 16, v110
	v_cndmask_b32_e32 v55, v55, v57, vcc
	v_sqrt_f32_e32 v57, v55
	s_nop 0
	v_add_u32_e32 v127, -1, v57
	v_fma_f32 v129, -v127, v57, v55
	v_cmp_ge_f32_e64 s[4:5], 0, v129
	v_add_u32_e32 v129, 1, v57
	s_nop 0
	v_cndmask_b32_e64 v127, v57, v127, s[4:5]
	v_fma_f32 v57, -v129, v57, v55
	v_cmp_lt_f32_e64 s[4:5], 0, v57
	s_nop 1
	v_cndmask_b32_e64 v57, v127, v129, s[4:5]
	v_mul_f32_e32 v127, 0x37800000, v57
	v_cndmask_b32_e32 v57, v57, v127, vcc
	v_cmp_class_f32_e32 vcc, v55, v126
	v_and_b32_e32 v129, 0xffff0000, v110
	v_lshlrev_b32_e32 v110, 16, v111
	v_cndmask_b32_e32 v55, v57, v55, vcc
	v_div_scale_f32 v57, s[4:5], v55, v55, -1.0
	v_rcp_f32_e32 v127, v57
	v_and_b32_e32 v111, 0xffff0000, v111
	v_pk_add_f32 v[138:139], v[128:129], -1.0 op_sel_hi:[1,0]
	v_fma_f32 v134, -v57, v127, 1.0
	v_fmac_f32_e32 v127, v134, v127
	v_div_scale_f32 v134, vcc, -1.0, v55, -1.0
	v_mul_f32_e32 v135, v134, v127
	v_fma_f32 v136, -v57, v135, v134
	v_fmac_f32_e32 v135, v136, v127
	v_fma_f32 v57, -v57, v135, v134
	v_pk_add_f32 v[136:137], v[110:111], -1.0 op_sel_hi:[1,0]
	v_pk_fma_f32 v[138:139], v[18:19], v[138:139], 1.0 op_sel_hi:[1,1,0]
	v_div_fmas_f32 v57, v57, v127, v135
	v_pk_fma_f32 v[136:137], v[20:21], v[136:137], 1.0 op_sel_hi:[1,1,0]
	v_pk_mul_f32 v[122:123], v[138:139], v[122:123]
	v_bfe_u32 v127, v120, 16, 1
	v_pk_mul_f32 v[114:115], v[136:137], v[114:115]
	v_pk_mul_f32 v[136:137], v[120:121], v[122:123]
	v_add3_u32 v120, v120, v127, s59
	v_bfe_u32 v127, v121, 16, 1
	v_lshrrev_b32_e32 v120, 16, v120
	v_add3_u32 v121, v121, v127, s59
	v_and_or_b32 v120, v121, s7, v120
	v_bfe_u32 v121, v116, 16, 1
	v_pk_mul_f32 v[138:139], v[116:117], v[114:115]
	v_add3_u32 v116, v116, v121, s59
	v_bfe_u32 v121, v117, 16, 1
	v_pk_mul_f32 v[136:137], v[22:23], v[136:137]
	v_lshrrev_b32_e32 v116, 16, v116
	v_add3_u32 v117, v117, v121, s59
	v_div_fixup_f32 v134, v57, v55, -1.0
	v_add_f32_e32 v55, v136, v137
	v_lshl_add_u64 v[136:137], s[68:69], 0, v[62:63]
	v_and_or_b32 v121, v117, s7, v116
	v_lshl_add_u64 v[116:117], s[68:69], 0, v[60:61]
	s_waitcnt vmcnt(0)
	global_store_dwordx4 v[136:137], v[38:41], off nt
	global_store_dwordx2 v[116:117], v[120:121], off offset:-128 nt
	v_bfe_u32 v120, v122, 16, 1
	v_add3_u32 v120, v122, v120, s59
	v_bfe_u32 v121, v123, 16, 1
	v_lshrrev_b32_e32 v120, 16, v120
	v_add3_u32 v121, v123, v121, s59
	v_and_or_b32 v120, v121, s7, v120
	v_bfe_u32 v121, v114, 16, 1
	v_add3_u32 v114, v114, v121, s59
	v_bfe_u32 v121, v115, 16, 1
	v_lshrrev_b32_e32 v114, 16, v114
	v_add3_u32 v115, v115, v121, s59
	v_and_or_b32 v121, v115, s7, v114
	v_bfe_u32 v114, v118, 16, 1
	v_add3_u32 v114, v118, v114, s59
	v_bfe_u32 v115, v119, 16, 1
	v_lshrrev_b32_e32 v114, 16, v114
	v_add3_u32 v115, v119, v115, s59
	v_and_or_b32 v114, v115, s7, v114
	v_bfe_u32 v115, v112, 16, 1
	v_add3_u32 v112, v112, v115, s59
	v_bfe_u32 v115, v113, 16, 1
	v_pk_mul_f32 v[40:41], v[130:131], v[134:135] op_sel_hi:[1,0]
	v_lshrrev_b32_e32 v112, 16, v112
	v_add3_u32 v113, v113, v115, s59
	v_and_or_b32 v115, v113, s7, v112
	v_bfe_u32 v112, v40, 16, 1
	v_pk_mul_f32 v[128:129], v[40:41], v[128:129] neg_lo:[1,0] neg_hi:[1,0]
	v_add3_u32 v40, v40, v112, s59
	v_bfe_u32 v112, v41, 16, 1
	v_pk_mul_f32 v[38:39], v[132:133], v[134:135] op_sel_hi:[1,0]
	v_lshrrev_b32_e32 v40, 16, v40
	v_add3_u32 v41, v41, v112, s59
	v_and_or_b32 v40, v41, s7, v40
	v_bfe_u32 v41, v38, 16, 1
	v_pk_mul_f32 v[110:111], v[38:39], v[110:111] neg_lo:[1,0] neg_hi:[1,0]
	v_add3_u32 v38, v38, v41, s59
	v_bfe_u32 v41, v39, 16, 1
	v_lshrrev_b32_e32 v38, 16, v38
	v_add3_u32 v39, v39, v41, s59
	v_pk_mul_f32 v[138:139], v[24:25], v[138:139]
	v_and_or_b32 v41, v39, s7, v38
	v_bfe_u32 v38, v128, 16, 1
	v_add_f32_e32 v57, v138, v139
	v_add3_u32 v38, v128, v38, s59
	v_bfe_u32 v39, v129, 16, 1
	v_add_f32_e32 v55, v55, v57
	v_lshrrev_b32_e32 v38, 16, v38
	v_add3_u32 v39, v129, v39, s59
	v_add_f32_dpp v55, v55, v55 quad_perm:[1,0,3,2] row_mask:0xf bank_mask:0xf bound_ctrl:1
	v_and_or_b32 v38, v39, s7, v38
	v_bfe_u32 v39, v110, 16, 1
	v_add_f32_dpp v55, v55, v55 quad_perm:[2,3,0,1] row_mask:0xf bank_mask:0xf bound_ctrl:1
	global_store_dwordx2 v[116:117], v[40:41], off offset:256 nt
	v_add3_u32 v39, v110, v39, s59
	v_bfe_u32 v40, v111, 16, 1
	v_add_f32_dpp v55, v55, v55 row_half_mirror row_mask:0xf bank_mask:0xf bound_ctrl:1
	v_mov_b32_e32 v57, 0
	v_lshrrev_b32_e32 v39, 16, v39
	v_add3_u32 v40, v111, v40, s59
	v_mov_b32_dpp v57, v55 row_mirror row_mask:0xf bank_mask:0xf
	v_and_or_b32 v39, v40, s7, v39
	global_store_dwordx2 v[116:117], v[120:121], off nt
	global_store_dwordx2 v[116:117], v[114:115], off offset:128 nt
	global_store_dwordx2 v[116:117], v[38:39], off offset:384 nt
	s_and_saveexec_b64 s[4:5], s[0:1]
	s_cbranch_execz .LBB0_1876
	v_add_f32_e32 v40, v55, v57
	v_ashrrev_i32_e32 v55, 31, v54
	v_lshl_add_u64 v[38:39], v[54:55], 2, s[10:11]
	global_store_dword v[38:39], v40, off
	s_or_b64 exec, exec, s[4:5]
	s_andn2_b64 vcc, exec, s[54:55]
	s_cbranch_vccz .LBB0_1877

; __device__ __forceinline__ unsigned pk2(float lo, float hi) { return f2bf(lo) | (f2bf(hi) << 16); }
; __device__ __forceinline__ f32x4 bf4(v2u w) { return (f32x4){bflo(w.x), bfhi(w.x), bflo(w.y), bfhi(w.y)}; }
; __device__ __forceinline__ void p4_rwkv_prep(Frame& F) {
;     ...
;         for (int k = 0; k < 4; ++k) { const int t = tb + k * tstep;
;             if (t < S_) {
;                 const f32x4 rc = bf4(zcr[k]), kc = bf4(zck[k]), vc = bf4(zcv[k]);
;                 f32x4 rp = {0.f, 0.f, 0.f, 0.f}, kp = rp, vp = rp;
;                 if (t > 0) { rp = bf4(zpr[k]); kp = bf4(zpk[k]); vp = bf4(zpv[k]); }
;                 const f32x4 r = rc + (rp - rc) * mur, kx = kc + (kp - kc) * muk, v = vc + (vp - vc) * muv;
;                 const f32x4 iclr = bf4(ic[k]), w = wd[k];
;                 f32x4 kk = kx * kk4;
;                 const float ss = dpp_add16((kk.x * kk.x + kk.y * kk.y) + (kk.z * kk.z + kk.w * kk.w)); kk = kk * (1.0f / sqrtf(ss + 1e-12f));
;                 const f32x4 km = kx * (1.0f + (iclr - 1.0f) * ka4);
;                 const f32x4 rkr = r * km * rk4;
;                 const float bc = dpp_add16((rkr.x + rkr.y) + (rkr.z + rkr.w));
;                 unsigned char* rec = SC + ((size_t)h * S_ + t) * SCAN_REC;
;                 *(f32x4*)(rec + 16 * q) = w;
;                 const f32x4 a = -kk, b = kk * iclr;
;                 *(v2u*)(rec + 256 + 8 * q) = (v2u){pk2(r.x, r.y), pk2(r.z, r.w)};
;                 *(v2u*)(rec + 384 + 8 * q) = (v2u){pk2(km.x, km.y), pk2(km.z, km.w)};
;                 *(v2u*)(rec + 512 + 8 * q) = (v2u){pk2(v.x, v.y), pk2(v.z, v.w)};
;                 *(v2u*)(rec + 640 + 8 * q) = (v2u){pk2(a.x, a.y), pk2(a.z, a.w)};
;                 *(v2u*)(rec + 768 + 8 * q) = (v2u){pk2(b.x, b.y), pk2(b.z, b.w)};
;                 if (q == 0) BC[t * RH + h] = bc; } }
.LBB0_1880:
	v_lshlrev_b32_e32 v92, 16, v84
	v_and_b32_e32 v93, 0xffff0000, v84
	v_lshlrev_b32_e32 v84, 16, v85
	v_and_b32_e32 v85, 0xffff0000, v85
	v_lshlrev_b32_e32 v94, 16, v86
	v_and_b32_e32 v95, 0xffff0000, v86
	v_lshlrev_b32_e32 v86, 16, v87
	v_and_b32_e32 v87, 0xffff0000, v87
	v_sub_f32_e32 v99, v90, v93
	v_sub_f32_e32 v98, v55, v92
	v_sub_f32_e32 v91, v91, v85
	v_sub_f32_e32 v90, v57, v84
	v_pk_fma_f32 v[84:85], v[4:5], v[90:91], v[84:85]
	v_pk_fma_f32 v[90:91], v[2:3], v[98:99], v[92:93]
	v_sub_f32_e32 v93, v40, v95
	v_sub_f32_e32 v92, v38, v94
	v_sub_f32_e32 v41, v41, v87
	v_sub_f32_e32 v40, v39, v86
	v_pk_fma_f32 v[38:39], v[8:9], v[40:41], v[86:87]
	v_pk_fma_f32 v[40:41], v[6:7], v[92:93], v[94:95]
	v_lshlrev_b32_e32 v96, 16, v88
	v_and_b32_e32 v97, 0xffff0000, v88
	v_lshlrev_b32_e32 v88, 16, v89
	v_pk_mul_f32 v[92:93], v[14:15], v[40:41]
	v_pk_mul_f32 v[94:95], v[16:17], v[38:39]
	v_sub_f32_e32 v87, v36, v97
	v_sub_f32_e32 v86, v34, v96
	v_sub_f32_e32 v36, v35, v88
	v_pk_mul_f32 v[34:35], v[94:95], v[94:95]
	v_pk_mul_f32 v[98:99], v[92:93], v[92:93]
	v_pk_fma_f32 v[86:87], v[10:11], v[86:87], v[96:97]
	v_pk_mov_b32 v[100:101], v[98:99], v[34:35] op_sel:[1,0]
	v_mov_b32_e32 v99, v35
	v_pk_add_f32 v[34:35], v[100:101], v[98:99]
	v_and_b32_e32 v89, 0xffff0000, v89
	v_add_f32_e32 v34, v34, v35
	v_sub_f32_e32 v37, v37, v89
	v_pk_fma_f32 v[36:37], v[12:13], v[36:37], v[88:89]
	v_add_f32_dpp v34, v34, v34 quad_perm:[1,0,3,2] row_mask:0xf bank_mask:0xf bound_ctrl:1
	v_lshlrev_b32_e32 v88, 16, v82
	v_and_b32_e32 v89, 0xffff0000, v82
	v_add_f32_dpp v34, v34, v34 quad_perm:[2,3,0,1] row_mask:0xf bank_mask:0xf bound_ctrl:1
	v_lshlrev_b32_e32 v82, 16, v83
	v_and_b32_e32 v83, 0xffff0000, v83
	v_add_f32_dpp v34, v34, v34 row_half_mirror row_mask:0xf bank_mask:0xf bound_ctrl:1
	v_pk_add_f32 v[98:99], v[88:89], -1.0 op_sel_hi:[1,0]
	s_ashr_i32 s47, s46, 31
	v_add_f32_dpp v34, v34, v34 row_mirror row_mask:0xf bank_mask:0xf bound_ctrl:1
	v_add_f32_e32 v34, 0x2b8cbccc, v34
	v_mul_f32_e32 v35, 0x4f800000, v34
	v_cmp_gt_f32_e32 vcc, s29, v34
	v_pk_fma_f32 v[98:99], v[18:19], v[98:99], 1.0 op_sel_hi:[1,1,0]
	v_mov_b64_e32 v[100:101], s[8:9]
	v_cndmask_b32_e32 v34, v34, v35, vcc
	v_sqrt_f32_e32 v35, v34
	v_pk_mul_f32 v[40:41], v[98:99], v[40:41]
	v_add_u32_e32 v55, -1, v35
	v_fma_f32 v57, -v55, v35, v34
	v_cmp_ge_f32_e64 s[4:5], 0, v57
	v_add_u32_e32 v57, 1, v35
	s_nop 0
	v_cndmask_b32_e64 v55, v35, v55, s[4:5]
	v_fma_f32 v35, -v57, v35, v34
	v_cmp_lt_f32_e64 s[4:5], 0, v35
	s_nop 1
	v_cndmask_b32_e64 v35, v55, v57, s[4:5]
	v_mul_f32_e32 v55, 0x37800000, v35
	v_cndmask_b32_e32 v35, v35, v55, vcc
	v_cmp_class_f32_e32 vcc, v34, v126
	s_nop 1
	v_cndmask_b32_e32 v34, v35, v34, vcc
	v_div_scale_f32 v35, s[4:5], v34, v34, -1.0
	v_rcp_f32_e32 v55, v35
	s_nop 0
	v_fma_f32 v57, -v35, v55, 1.0
	v_fmac_f32_e32 v55, v57, v55
	v_div_scale_f32 v57, vcc, -1.0, v34, -1.0
	v_mul_f32_e32 v96, v57, v55
	v_fma_f32 v97, -v35, v96, v57
	v_fmac_f32_e32 v96, v97, v55
	v_fma_f32 v35, -v35, v96, v57
	v_div_fmas_f32 v35, v35, v55, v96
	v_bfe_u32 v55, v90, 16, 1
	v_div_fixup_f32 v96, v35, v34, -1.0
	v_pk_add_f32 v[34:35], v[82:83], -1.0 op_sel_hi:[1,0]
	v_add3_u32 v55, v90, v55, s59
	v_bfe_u32 v57, v91, 16, 1
	v_pk_fma_f32 v[34:35], v[20:21], v[34:35], 1.0 op_sel_hi:[1,1,0]
	v_lshrrev_b32_e32 v55, 16, v55
	v_add3_u32 v57, v91, v57, s59
	v_pk_mul_f32 v[38:39], v[34:35], v[38:39]
	v_pk_mul_f32 v[34:35], v[90:91], v[40:41]
	v_and_or_b32 v90, v57, s7, v55
	v_bfe_u32 v55, v84, 16, 1
	v_add3_u32 v55, v84, v55, s59
	v_bfe_u32 v57, v85, 16, 1
	v_lshrrev_b32_e32 v55, 16, v55
	v_add3_u32 v57, v85, v57, s59
	v_and_or_b32 v91, v57, s7, v55
	v_bfe_u32 v55, v40, 16, 1
	v_add3_u32 v40, v40, v55, s59
	v_bfe_u32 v55, v41, 16, 1
	v_lshrrev_b32_e32 v40, 16, v40
	v_add3_u32 v41, v41, v55, s59
	v_and_or_b32 v40, v41, s7, v40
	v_bfe_u32 v41, v38, 16, 1
	v_pk_mul_f32 v[98:99], v[84:85], v[38:39]
	v_add3_u32 v38, v38, v41, s59
	v_bfe_u32 v41, v39, 16, 1
	v_lshrrev_b32_e32 v38, 16, v38
	v_add3_u32 v39, v39, v41, s59
	v_pk_mul_f32 v[98:99], v[24:25], v[98:99]
	v_pk_mul_f32 v[34:35], v[22:23], v[34:35]
	v_and_or_b32 v41, v39, s7, v38
	v_bfe_u32 v38, v86, 16, 1
	v_add_f32_e32 v34, v34, v35
	v_add_f32_e32 v35, v98, v99
	v_lshl_add_u64 v[98:99], v[48:49], 0, s[46:47]
	v_add3_u32 v38, v86, v38, s59
	v_bfe_u32 v39, v87, 16, 1
	v_mad_u64_u32 v[100:101], s[4:5], v98, s58, v[100:101]
	v_lshrrev_b32_e32 v38, 16, v38
	v_add3_u32 v39, v87, v39, s59
	v_mad_i32_i24 v101, v99, s58, v101
	v_and_or_b32 v38, v39, s7, v38
	v_bfe_u32 v39, v36, 16, 1
	v_lshl_add_u64 v[98:99], v[100:101], 0, v[50:51]
	v_add3_u32 v36, v36, v39, s59
	v_bfe_u32 v39, v37, 16, 1
	global_store_dwordx4 v[98:99], v[30:33], off nt
	v_lshrrev_b32_e32 v36, 16, v36
	v_add3_u32 v37, v37, v39, s59
	v_pk_mul_f32 v[32:33], v[92:93], v[96:97] op_sel_hi:[1,0]
	v_and_or_b32 v39, v37, s7, v36
	v_bfe_u32 v36, v32, 16, 1
	v_pk_mul_f32 v[88:89], v[32:33], v[88:89] neg_lo:[1,0] neg_hi:[1,0]
	v_add3_u32 v32, v32, v36, s59
	v_bfe_u32 v36, v33, 16, 1
	v_pk_mul_f32 v[30:31], v[94:95], v[96:97] op_sel_hi:[1,0]
	v_lshrrev_b32_e32 v32, 16, v32
	v_add3_u32 v33, v33, v36, s59
	v_and_or_b32 v32, v33, s7, v32
	v_bfe_u32 v33, v30, 16, 1
	v_pk_mul_f32 v[82:83], v[30:31], v[82:83] neg_lo:[1,0] neg_hi:[1,0]
	v_add3_u32 v30, v30, v33, s59
	v_bfe_u32 v33, v31, 16, 1
	v_lshrrev_b32_e32 v30, 16, v30
	v_add3_u32 v31, v31, v33, s59
	v_and_or_b32 v33, v31, s7, v30
	v_bfe_u32 v30, v88, 16, 1
	v_add3_u32 v30, v88, v30, s59
	v_bfe_u32 v31, v89, 16, 1
	v_add_f32_e32 v34, v34, v35
	v_lshrrev_b32_e32 v30, 16, v30
	v_add3_u32 v31, v89, v31, s59
	v_add_f32_dpp v34, v34, v34 quad_perm:[1,0,3,2] row_mask:0xf bank_mask:0xf bound_ctrl:1
	v_lshl_add_u64 v[84:85], v[100:101], 0, v[52:53]
	v_and_or_b32 v30, v31, s7, v30
	v_bfe_u32 v31, v82, 16, 1
	v_add_f32_dpp v34, v34, v34 quad_perm:[2,3,0,1] row_mask:0xf bank_mask:0xf bound_ctrl:1
	global_store_dwordx2 v[84:85], v[32:33], off offset:640 nt
	v_add3_u32 v31, v82, v31, s59
	v_bfe_u32 v32, v83, 16, 1
	v_add_f32_dpp v34, v34, v34 row_half_mirror row_mask:0xf bank_mask:0xf bound_ctrl:1
	v_mov_b32_e32 v35, 0
	v_lshrrev_b32_e32 v31, 16, v31
	v_add3_u32 v32, v83, v32, s59
	v_mov_b32_dpp v35, v34 row_mirror row_mask:0xf bank_mask:0xf
	v_and_or_b32 v31, v32, s7, v31
	global_store_dwordx2 v[84:85], v[90:91], off offset:256 nt
	global_store_dwordx2 v[84:85], v[40:41], off offset:384 nt
	global_store_dwordx2 v[84:85], v[38:39], off offset:512 nt
	global_store_dwordx2 v[84:85], v[30:31], off offset:768 nt
	s_and_saveexec_b64 s[4:5], s[0:1]
	s_cbranch_execz .LBB0_1882
	v_add_u32_e32 v30, s35, v54
	v_ashrrev_i32_e32 v31, 31, v30
	v_add_f32_e32 v32, v34, v35
	v_lshl_add_u64 v[30:31], v[30:31], 2, s[10:11]
	global_store_dword v[30:31], v32, off

; __device__ __forceinline__ unsigned pk2(float lo, float hi) { return f2bf(lo) | (f2bf(hi) << 16); }
; __device__ __forceinline__ f32x4 bf4(v2u w) { return (f32x4){bflo(w.x), bfhi(w.x), bflo(w.y), bfhi(w.y)}; }
; __device__ __forceinline__ void p4_rwkv_prep(Frame& F) {
;     ...
;         for (int k = 0; k < 4; ++k) { const int t = tb + k * tstep;
;             if (t < S_) {
;                 const f32x4 rc = bf4(zcr[k]), kc = bf4(zck[k]), vc = bf4(zcv[k]);
;                 f32x4 rp = {0.f, 0.f, 0.f, 0.f}, kp = rp, vp = rp;
;                 if (t > 0) { rp = bf4(zpr[k]); kp = bf4(zpk[k]); vp = bf4(zpv[k]); }
;                 const f32x4 r = rc + (rp - rc) * mur, kx = kc + (kp - kc) * muk, v = vc + (vp - vc) * muv;
;                 const f32x4 iclr = bf4(ic[k]), w = wd[k];
;                 f32x4 kk = kx * kk4;
;                 const float ss = dpp_add16((kk.x * kk.x + kk.y * kk.y) + (kk.z * kk.z + kk.w * kk.w)); kk = kk * (1.0f / sqrtf(ss + 1e-12f));
;                 const f32x4 km = kx * (1.0f + (iclr - 1.0f) * ka4);
;                 const f32x4 rkr = r * km * rk4;
;                 const float bc = dpp_add16((rkr.x + rkr.y) + (rkr.z + rkr.w));
;                 unsigned char* rec = SC + ((size_t)h * S_ + t) * SCAN_REC;
;                 *(f32x4*)(rec + 16 * q) = w;
;                 const f32x4 a = -kk, b = kk * iclr;
;                 *(v2u*)(rec + 256 + 8 * q) = (v2u){pk2(r.x, r.y), pk2(r.z, r.w)};
;                 *(v2u*)(rec + 384 + 8 * q) = (v2u){pk2(km.x, km.y), pk2(km.z, km.w)};
;                 *(v2u*)(rec + 512 + 8 * q) = (v2u){pk2(v.x, v.y), pk2(v.z, v.w)};
;                 *(v2u*)(rec + 640 + 8 * q) = (v2u){pk2(a.x, a.y), pk2(a.z, a.w)};
;                 *(v2u*)(rec + 768 + 8 * q) = (v2u){pk2(b.x, b.y), pk2(b.z, b.w)};
;                 if (q == 0) BC[t * RH + h] = bc; } }
.LBB0_1884:
	v_lshlrev_b32_e32 v106, 16, v98
	v_and_b32_e32 v107, 0xffff0000, v98
	v_lshlrev_b32_e32 v98, 16, v99
	v_lshlrev_b32_e32 v108, 16, v100
	v_and_b32_e32 v109, 0xffff0000, v100
	v_lshlrev_b32_e32 v100, 16, v101
	v_and_b32_e32 v101, 0xffff0000, v101
	v_and_b32_e32 v99, 0xffff0000, v99
	v_sub_f32_e32 v117, v112, v107
	v_sub_f32_e32 v116, v110, v106
	v_sub_f32_e32 v112, v111, v98
	v_sub_f32_e32 v111, v104, v109
	v_sub_f32_e32 v110, v55, v108
	v_sub_f32_e32 v105, v105, v101
	v_sub_f32_e32 v104, v57, v100
	v_sub_f32_e32 v113, v113, v99
	v_pk_fma_f32 v[100:101], v[8:9], v[104:105], v[100:101]
	v_pk_fma_f32 v[104:105], v[6:7], v[110:111], v[108:109]
	v_lshlrev_b32_e32 v114, 16, v102
	v_and_b32_e32 v115, 0xffff0000, v102
	v_lshlrev_b32_e32 v102, 16, v103
	v_pk_fma_f32 v[98:99], v[4:5], v[112:113], v[98:99]
	v_pk_mul_f32 v[110:111], v[14:15], v[104:105]
	v_pk_mul_f32 v[112:113], v[16:17], v[100:101]
	v_pk_fma_f32 v[106:107], v[2:3], v[116:117], v[106:107]
	v_sub_f32_e32 v109, v40, v115
	v_sub_f32_e32 v108, v38, v114
	v_sub_f32_e32 v40, v39, v102
	v_pk_mul_f32 v[38:39], v[112:113], v[112:113]
	v_pk_mul_f32 v[116:117], v[110:111], v[110:111]
	v_and_b32_e32 v103, 0xffff0000, v103
	v_pk_mov_b32 v[118:119], v[116:117], v[38:39] op_sel:[1,0]
	v_mov_b32_e32 v117, v39
	v_pk_add_f32 v[38:39], v[118:119], v[116:117]
	v_sub_f32_e32 v41, v41, v103
	v_add_f32_e32 v38, v38, v39
	v_pk_fma_f32 v[40:41], v[12:13], v[40:41], v[102:103]
	v_pk_fma_f32 v[102:103], v[10:11], v[108:109], v[114:115]
	v_add_f32_dpp v38, v38, v38 quad_perm:[1,0,3,2] row_mask:0xf bank_mask:0xf bound_ctrl:1
	v_lshlrev_b32_e32 v108, 16, v96
	v_and_b32_e32 v109, 0xffff0000, v96
	v_add_f32_dpp v38, v38, v38 quad_perm:[2,3,0,1] row_mask:0xf bank_mask:0xf bound_ctrl:1
	v_lshlrev_b32_e32 v96, 16, v97
	v_and_b32_e32 v97, 0xffff0000, v97
	v_add_f32_dpp v38, v38, v38 row_half_mirror row_mask:0xf bank_mask:0xf bound_ctrl:1
	v_pk_add_f32 v[116:117], v[108:109], -1.0 op_sel_hi:[1,0]
	s_ashr_i32 s51, s50, 31
	v_add_f32_dpp v38, v38, v38 row_mirror row_mask:0xf bank_mask:0xf bound_ctrl:1
	v_add_f32_e32 v38, 0x2b8cbccc, v38
	v_mul_f32_e32 v39, 0x4f800000, v38
	v_cmp_gt_f32_e32 vcc, s29, v38
	v_pk_fma_f32 v[116:117], v[18:19], v[116:117], 1.0 op_sel_hi:[1,1,0]
	v_mov_b64_e32 v[118:119], s[8:9]
	v_cndmask_b32_e32 v38, v38, v39, vcc
	v_sqrt_f32_e32 v39, v38
	v_pk_mul_f32 v[104:105], v[116:117], v[104:105]
	v_add_u32_e32 v55, -1, v39
	v_fma_f32 v57, -v55, v39, v38
	v_cmp_ge_f32_e64 s[4:5], 0, v57
	v_add_u32_e32 v57, 1, v39
	s_nop 0
	v_cndmask_b32_e64 v55, v39, v55, s[4:5]
	v_fma_f32 v39, -v57, v39, v38
	v_cmp_lt_f32_e64 s[4:5], 0, v39
	s_nop 1
	v_cndmask_b32_e64 v39, v55, v57, s[4:5]
	v_mul_f32_e32 v55, 0x37800000, v39
	v_cndmask_b32_e32 v39, v39, v55, vcc
	v_cmp_class_f32_e32 vcc, v38, v126
	s_nop 1
	v_cndmask_b32_e32 v38, v39, v38, vcc
	v_div_scale_f32 v39, s[4:5], v38, v38, -1.0
	v_rcp_f32_e32 v55, v39
	s_nop 0
	v_fma_f32 v57, -v39, v55, 1.0
	v_fmac_f32_e32 v55, v57, v55
	v_div_scale_f32 v57, vcc, -1.0, v38, -1.0
	v_mul_f32_e32 v114, v57, v55
	v_fma_f32 v115, -v39, v114, v57
	v_fmac_f32_e32 v114, v115, v55
	v_fma_f32 v39, -v39, v114, v57
	v_div_fmas_f32 v39, v39, v55, v114
	v_bfe_u32 v55, v106, 16, 1
	v_div_fixup_f32 v114, v39, v38, -1.0
	v_pk_add_f32 v[38:39], v[96:97], -1.0 op_sel_hi:[1,0]
	v_add3_u32 v55, v106, v55, s59
	v_bfe_u32 v57, v107, 16, 1
	v_pk_fma_f32 v[38:39], v[20:21], v[38:39], 1.0 op_sel_hi:[1,1,0]
	v_lshrrev_b32_e32 v55, 16, v55
	v_add3_u32 v57, v107, v57, s59
	v_pk_mul_f32 v[100:101], v[38:39], v[100:101]
	v_pk_mul_f32 v[38:39], v[106:107], v[104:105]
	v_and_or_b32 v106, v57, s7, v55
	v_bfe_u32 v55, v98, 16, 1
	v_add3_u32 v55, v98, v55, s59
	v_bfe_u32 v57, v99, 16, 1
	v_lshrrev_b32_e32 v55, 16, v55
	v_add3_u32 v57, v99, v57, s59
	v_and_or_b32 v107, v57, s7, v55
	v_bfe_u32 v55, v104, 16, 1
	v_add3_u32 v55, v104, v55, s59
	v_bfe_u32 v57, v105, 16, 1
	v_lshrrev_b32_e32 v55, 16, v55
	v_add3_u32 v57, v105, v57, s59
	v_and_or_b32 v104, v57, s7, v55
	v_bfe_u32 v55, v100, 16, 1
	v_add3_u32 v55, v100, v55, s59
	v_bfe_u32 v57, v101, 16, 1
	v_pk_mul_f32 v[116:117], v[98:99], v[100:101]
	v_lshrrev_b32_e32 v55, 16, v55
	v_add3_u32 v57, v101, v57, s59
	v_pk_mul_f32 v[116:117], v[24:25], v[116:117]
	v_pk_mul_f32 v[38:39], v[22:23], v[38:39]
	v_and_or_b32 v105, v57, s7, v55
	v_bfe_u32 v55, v102, 16, 1
	v_add_f32_e32 v38, v38, v39
	v_add_f32_e32 v39, v116, v117
	v_lshl_add_u64 v[116:117], v[48:49], 0, s[50:51]
	v_add3_u32 v55, v102, v55, s59
	v_bfe_u32 v57, v103, 16, 1
	v_mad_u64_u32 v[118:119], s[4:5], v116, s58, v[118:119]
	v_lshrrev_b32_e32 v55, 16, v55
	v_add3_u32 v57, v103, v57, s59
	v_mad_i32_i24 v119, v117, s58, v119
	v_and_or_b32 v100, v57, s7, v55
	v_bfe_u32 v55, v40, 16, 1
	v_lshl_add_u64 v[116:117], v[118:119], 0, v[50:51]
	v_add3_u32 v40, v40, v55, s59
	v_bfe_u32 v55, v41, 16, 1
	global_store_dwordx4 v[116:117], v[34:37], off nt
	v_lshrrev_b32_e32 v40, 16, v40
	v_add3_u32 v41, v41, v55, s59
	v_pk_mul_f32 v[36:37], v[110:111], v[114:115] op_sel_hi:[1,0]
	v_and_or_b32 v101, v41, s7, v40
	v_bfe_u32 v40, v36, 16, 1
	v_pk_mul_f32 v[108:109], v[36:37], v[108:109] neg_lo:[1,0] neg_hi:[1,0]
	v_add3_u32 v36, v36, v40, s59
	v_bfe_u32 v40, v37, 16, 1
	v_pk_mul_f32 v[34:35], v[112:113], v[114:115] op_sel_hi:[1,0]
	v_lshrrev_b32_e32 v36, 16, v36
	v_add3_u32 v37, v37, v40, s59
	v_and_or_b32 v36, v37, s7, v36
	v_bfe_u32 v37, v34, 16, 1
	v_pk_mul_f32 v[96:97], v[34:35], v[96:97] neg_lo:[1,0] neg_hi:[1,0]
	v_add3_u32 v34, v34, v37, s59
	v_bfe_u32 v37, v35, 16, 1
	v_lshrrev_b32_e32 v34, 16, v34
	v_add3_u32 v35, v35, v37, s59
	v_and_or_b32 v37, v35, s7, v34
	v_bfe_u32 v34, v108, 16, 1
	v_add3_u32 v34, v108, v34, s59
	v_bfe_u32 v35, v109, 16, 1
	v_add_f32_e32 v38, v38, v39
	v_lshrrev_b32_e32 v34, 16, v34
	v_add3_u32 v35, v109, v35, s59
	v_add_f32_dpp v38, v38, v38 quad_perm:[1,0,3,2] row_mask:0xf bank_mask:0xf bound_ctrl:1
	v_lshl_add_u64 v[98:99], v[118:119], 0, v[52:53]
	v_and_or_b32 v34, v35, s7, v34
	v_bfe_u32 v35, v96, 16, 1
	v_add_f32_dpp v38, v38, v38 quad_perm:[2,3,0,1] row_mask:0xf bank_mask:0xf bound_ctrl:1
	global_store_dwordx2 v[98:99], v[36:37], off offset:640 nt
	v_add3_u32 v35, v96, v35, s59
	v_bfe_u32 v36, v97, 16, 1
	v_add_f32_dpp v38, v38, v38 row_half_mirror row_mask:0xf bank_mask:0xf bound_ctrl:1
	v_mov_b32_e32 v39, 0
	v_lshrrev_b32_e32 v35, 16, v35
	v_add3_u32 v36, v97, v36, s59
	v_mov_b32_dpp v39, v38 row_mirror row_mask:0xf bank_mask:0xf
	v_and_or_b32 v35, v36, s7, v35
	global_store_dwordx2 v[98:99], v[106:107], off offset:256 nt
	global_store_dwordx2 v[98:99], v[104:105], off offset:384 nt
	global_store_dwordx2 v[98:99], v[100:101], off offset:512 nt
	global_store_dwordx2 v[98:99], v[34:35], off offset:768 nt
	s_and_saveexec_b64 s[4:5], s[0:1]
	s_cbranch_execz .LBB0_1886
	v_ashrrev_i32_e32 v57, 31, v56
	v_add_f32_e32 v36, v38, v39
	v_lshl_add_u64 v[34:35], v[56:57], 2, s[10:11]
	global_store_dword v[34:35], v36, off

; __device__ __forceinline__ unsigned pk2(float lo, float hi) { return f2bf(lo) | (f2bf(hi) << 16); }
; __device__ __forceinline__ f32x4 bf4(v2u w) { return (f32x4){bflo(w.x), bfhi(w.x), bflo(w.y), bfhi(w.y)}; }
; __device__ __forceinline__ void p4_rwkv_prep(Frame& F) {
;     ...
;         for (int k = 0; k < 4; ++k) { const int t = tb + k * tstep;
;             if (t < S_) {
;                 const f32x4 rc = bf4(zcr[k]), kc = bf4(zck[k]), vc = bf4(zcv[k]);
;                 f32x4 rp = {0.f, 0.f, 0.f, 0.f}, kp = rp, vp = rp;
;                 if (t > 0) { rp = bf4(zpr[k]); kp = bf4(zpk[k]); vp = bf4(zpv[k]); }
;                 const f32x4 r = rc + (rp - rc) * mur, kx = kc + (kp - kc) * muk, v = vc + (vp - vc) * muv;
;                 const f32x4 iclr = bf4(ic[k]), w = wd[k];
;                 f32x4 kk = kx * kk4;
;                 const float ss = dpp_add16((kk.x * kk.x + kk.y * kk.y) + (kk.z * kk.z + kk.w * kk.w)); kk = kk * (1.0f / sqrtf(ss + 1e-12f));
;                 const f32x4 km = kx * (1.0f + (iclr - 1.0f) * ka4);
;                 const f32x4 rkr = r * km * rk4;
;                 const float bc = dpp_add16((rkr.x + rkr.y) + (rkr.z + rkr.w));
;                 unsigned char* rec = SC + ((size_t)h * S_ + t) * SCAN_REC;
;                 *(f32x4*)(rec + 16 * q) = w;
;                 const f32x4 a = -kk, b = kk * iclr;
;                 *(v2u*)(rec + 256 + 8 * q) = (v2u){pk2(r.x, r.y), pk2(r.z, r.w)};
;                 *(v2u*)(rec + 384 + 8 * q) = (v2u){pk2(km.x, km.y), pk2(km.z, km.w)};
;                 *(v2u*)(rec + 512 + 8 * q) = (v2u){pk2(v.x, v.y), pk2(v.z, v.w)};
;                 *(v2u*)(rec + 640 + 8 * q) = (v2u){pk2(a.x, a.y), pk2(a.z, a.w)};
;                 *(v2u*)(rec + 768 + 8 * q) = (v2u){pk2(b.x, b.y), pk2(b.z, b.w)};
;                 if (q == 0) BC[t * RH + h] = bc; } }
.LBB0_1891:
	v_lshlrev_b32_e32 v76, 16, v70
	v_and_b32_e32 v77, 0xffff0000, v70
	v_lshlrev_b32_e32 v70, 16, v71
	v_and_b32_e32 v71, 0xffff0000, v71
	v_lshlrev_b32_e32 v78, 16, v72
	v_and_b32_e32 v79, 0xffff0000, v72
	v_lshlrev_b32_e32 v72, 16, v73
	v_and_b32_e32 v73, 0xffff0000, v73
	v_sub_f32_e32 v83, v40, v77
	v_sub_f32_e32 v41, v41, v71
	v_sub_f32_e32 v40, v39, v70
	v_sub_f32_e32 v82, v38, v76
	v_pk_fma_f32 v[38:39], v[4:5], v[40:41], v[70:71]
	v_sub_f32_e32 v71, v36, v79
	v_sub_f32_e32 v70, v34, v78
	v_sub_f32_e32 v37, v37, v73
	v_sub_f32_e32 v36, v35, v72
	v_pk_fma_f32 v[34:35], v[8:9], v[36:37], v[72:73]
	v_pk_fma_f32 v[36:37], v[6:7], v[70:71], v[78:79]
	v_lshlrev_b32_e32 v80, 16, v74
	v_and_b32_e32 v81, 0xffff0000, v74
	v_lshlrev_b32_e32 v74, 16, v75
	v_pk_fma_f32 v[40:41], v[2:3], v[82:83], v[76:77]
	v_pk_mul_f32 v[72:73], v[14:15], v[36:37]
	v_pk_mul_f32 v[76:77], v[16:17], v[34:35]
	v_sub_f32_e32 v71, v32, v81
	v_sub_f32_e32 v70, v30, v80
	v_sub_f32_e32 v32, v31, v74
	v_pk_mul_f32 v[30:31], v[76:77], v[76:77]
	v_pk_mul_f32 v[78:79], v[72:73], v[72:73]
	v_and_b32_e32 v75, 0xffff0000, v75
	v_pk_mov_b32 v[82:83], v[78:79], v[30:31] op_sel:[1,0]
	v_mov_b32_e32 v79, v31
	v_pk_add_f32 v[30:31], v[82:83], v[78:79]
	v_sub_f32_e32 v33, v33, v75
	v_add_f32_e32 v30, v30, v31
	v_pk_fma_f32 v[32:33], v[12:13], v[32:33], v[74:75]
	v_lshlrev_b32_e32 v74, 16, v68
	v_add_f32_dpp v30, v30, v30 quad_perm:[1,0,3,2] row_mask:0xf bank_mask:0xf bound_ctrl:1
	v_and_b32_e32 v75, 0xffff0000, v68
	v_lshlrev_b32_e32 v68, 16, v69
	v_add_f32_dpp v30, v30, v30 quad_perm:[2,3,0,1] row_mask:0xf bank_mask:0xf bound_ctrl:1
	v_and_b32_e32 v69, 0xffff0000, v69
	v_pk_fma_f32 v[70:71], v[10:11], v[70:71], v[80:81]
	v_add_f32_dpp v30, v30, v30 row_half_mirror row_mask:0xf bank_mask:0xf bound_ctrl:1
	v_pk_add_f32 v[80:81], v[74:75], -1.0 op_sel_hi:[1,0]
	s_ashr_i32 s45, s44, 31
	v_add_f32_dpp v30, v30, v30 row_mirror row_mask:0xf bank_mask:0xf bound_ctrl:1
	v_add_f32_e32 v30, 0x2b8cbccc, v30
	v_mul_f32_e32 v31, 0x4f800000, v30
	v_cmp_gt_f32_e32 vcc, s29, v30
	v_pk_fma_f32 v[80:81], v[18:19], v[80:81], 1.0 op_sel_hi:[1,1,0]
	v_mov_b64_e32 v[82:83], s[8:9]
	v_cndmask_b32_e32 v30, v30, v31, vcc
	v_sqrt_f32_e32 v31, v30
	v_pk_mul_f32 v[36:37], v[80:81], v[36:37]
	v_add_u32_e32 v55, -1, v31
	v_fma_f32 v57, -v55, v31, v30
	v_cmp_ge_f32_e64 s[4:5], 0, v57
	v_add_u32_e32 v57, 1, v31
	s_nop 0
	v_cndmask_b32_e64 v55, v31, v55, s[4:5]
	v_fma_f32 v31, -v57, v31, v30
	v_cmp_lt_f32_e64 s[4:5], 0, v31
	s_nop 1
	v_cndmask_b32_e64 v31, v55, v57, s[4:5]
	v_mul_f32_e32 v55, 0x37800000, v31
	v_cndmask_b32_e32 v31, v31, v55, vcc
	v_cmp_class_f32_e32 vcc, v30, v126
	s_nop 1
	v_cndmask_b32_e32 v30, v31, v30, vcc
	v_div_scale_f32 v31, s[4:5], v30, v30, -1.0
	v_rcp_f32_e32 v55, v31
	s_nop 0
	v_fma_f32 v57, -v31, v55, 1.0
	v_fmac_f32_e32 v55, v57, v55
	v_div_scale_f32 v57, vcc, -1.0, v30, -1.0
	v_mul_f32_e32 v78, v57, v55
	v_fma_f32 v79, -v31, v78, v57
	v_fmac_f32_e32 v78, v79, v55
	v_fma_f32 v31, -v31, v78, v57
	v_div_fmas_f32 v31, v31, v55, v78
	v_div_fixup_f32 v78, v31, v30, -1.0
	v_pk_add_f32 v[30:31], v[68:69], -1.0 op_sel_hi:[1,0]
	v_bfe_u32 v55, v40, 16, 1
	v_pk_fma_f32 v[30:31], v[20:21], v[30:31], 1.0 op_sel_hi:[1,1,0]
	s_nop 0
	v_pk_mul_f32 v[34:35], v[30:31], v[34:35]
	v_pk_mul_f32 v[30:31], v[40:41], v[36:37]
	v_pk_mul_f32 v[80:81], v[38:39], v[34:35]
	v_add3_u32 v40, v40, v55, s59
	v_bfe_u32 v55, v41, 16, 1
	v_pk_mul_f32 v[80:81], v[24:25], v[80:81]
	v_pk_mul_f32 v[30:31], v[22:23], v[30:31]
	v_lshrrev_b32_e32 v40, 16, v40
	v_add3_u32 v41, v41, v55, s59
	v_add_f32_e32 v30, v30, v31
	v_add_f32_e32 v31, v80, v81
	v_lshl_add_u64 v[80:81], v[48:49], 0, s[44:45]
	v_and_or_b32 v40, v41, s7, v40
	v_bfe_u32 v41, v38, 16, 1
	v_mad_u64_u32 v[82:83], s[4:5], v80, s58, v[82:83]
	v_add3_u32 v38, v38, v41, s59
	v_bfe_u32 v41, v39, 16, 1
	v_mad_i32_i24 v83, v81, s58, v83
	v_lshrrev_b32_e32 v38, 16, v38
	v_add3_u32 v39, v39, v41, s59
	v_and_or_b32 v41, v39, s7, v38
	v_lshl_add_u64 v[38:39], v[82:83], 0, v[52:53]
	global_store_dwordx2 v[38:39], v[40:41], off offset:256 nt
	v_bfe_u32 v40, v36, 16, 1
	v_add3_u32 v36, v36, v40, s59
	v_bfe_u32 v40, v37, 16, 1
	v_lshrrev_b32_e32 v36, 16, v36
	v_add3_u32 v37, v37, v40, s59
	v_and_or_b32 v36, v37, s7, v36
	v_bfe_u32 v37, v34, 16, 1
	v_add3_u32 v34, v34, v37, s59
	v_bfe_u32 v37, v35, 16, 1
	v_lshrrev_b32_e32 v34, 16, v34
	v_add3_u32 v35, v35, v37, s59
	v_and_or_b32 v37, v35, s7, v34
	v_bfe_u32 v34, v70, 16, 1
	v_add3_u32 v34, v70, v34, s59
	v_bfe_u32 v35, v71, 16, 1
	v_lshrrev_b32_e32 v34, 16, v34
	v_add3_u32 v35, v71, v35, s59
	v_and_or_b32 v34, v35, s7, v34
	v_bfe_u32 v35, v32, 16, 1
	v_lshl_add_u64 v[80:81], v[82:83], 0, v[50:51]
	v_add3_u32 v32, v32, v35, s59
	v_bfe_u32 v35, v33, 16, 1
	global_store_dwordx4 v[80:81], v[26:29], off nt
	v_lshrrev_b32_e32 v32, 16, v32
	v_add3_u32 v33, v33, v35, s59
	v_pk_mul_f32 v[28:29], v[72:73], v[78:79] op_sel_hi:[1,0]
	v_and_or_b32 v35, v33, s7, v32
	v_bfe_u32 v32, v28, 16, 1
	v_pk_mul_f32 v[72:73], v[28:29], v[74:75] neg_lo:[1,0] neg_hi:[1,0]
	v_add3_u32 v28, v28, v32, s59
	v_bfe_u32 v32, v29, 16, 1
	v_pk_mul_f32 v[26:27], v[76:77], v[78:79] op_sel_hi:[1,0]
	v_lshrrev_b32_e32 v28, 16, v28
	v_add3_u32 v29, v29, v32, s59
	v_and_or_b32 v28, v29, s7, v28
	v_bfe_u32 v29, v26, 16, 1
	v_pk_mul_f32 v[68:69], v[26:27], v[68:69] neg_lo:[1,0] neg_hi:[1,0]
	v_add3_u32 v26, v26, v29, s59
	v_bfe_u32 v29, v27, 16, 1
	v_lshrrev_b32_e32 v26, 16, v26
	v_add3_u32 v27, v27, v29, s59
	v_and_or_b32 v29, v27, s7, v26
	v_bfe_u32 v26, v72, 16, 1
	v_add3_u32 v26, v72, v26, s59
	v_bfe_u32 v27, v73, 16, 1
	v_add_f32_e32 v30, v30, v31
	v_lshrrev_b32_e32 v26, 16, v26
	v_add3_u32 v27, v73, v27, s59
	v_add_f32_dpp v30, v30, v30 quad_perm:[1,0,3,2] row_mask:0xf bank_mask:0xf bound_ctrl:1
	v_and_or_b32 v26, v27, s7, v26
	v_bfe_u32 v27, v68, 16, 1
	v_add_f32_dpp v30, v30, v30 quad_perm:[2,3,0,1] row_mask:0xf bank_mask:0xf bound_ctrl:1
	global_store_dwordx2 v[38:39], v[28:29], off offset:640 nt
	v_add3_u32 v27, v68, v27, s59
	v_bfe_u32 v28, v69, 16, 1
	v_add_f32_dpp v30, v30, v30 row_half_mirror row_mask:0xf bank_mask:0xf bound_ctrl:1
	v_mov_b32_e32 v31, 0
	v_lshrrev_b32_e32 v27, 16, v27
	v_add3_u32 v28, v69, v28, s59
	v_mov_b32_dpp v31, v30 row_mirror row_mask:0xf bank_mask:0xf
	v_and_or_b32 v27, v28, s7, v27
	global_store_dwordx2 v[38:39], v[36:37], off offset:384 nt
	global_store_dwordx2 v[38:39], v[34:35], off offset:512 nt
	global_store_dwordx2 v[38:39], v[26:27], off offset:768 nt
	s_and_saveexec_b64 s[4:5], s[0:1]
	s_cbranch_execz .LBB0_1846
	v_add_u32_e32 v26, s57, v54
	v_ashrrev_i32_e32 v27, 31, v26
	v_add_f32_e32 v28, v30, v31
	v_lshl_add_u64 v[26:27], v[26:27], 2, s[10:11]
	global_store_dword v[26:27], v28, off
	s_branch .LBB0_1846
